# speedup vs baseline: 1.0985x; 1.0119x over previous
_Z16chunksort_kernelPKiS0_PiS1_PKfPDF16_Pf:
	s_load_dwordx4 s[8:11], s[0:1], 0x0
	s_mul_i32 s4, s2, 0x7d0
	s_ashr_i32 s5, s4, 31
	s_lshl_b64 s[28:29], s[4:5], 4
	v_lshlrev_b32_e32 v1, 4, v0
	s_waitcnt lgkmcnt(0)
	s_add_u32 s4, s10, s28
	s_addc_u32 s5, s11, s29
	s_add_u32 s6, s8, s28
	s_addc_u32 s7, s9, s29
	global_load_dwordx4 v[10:13], v1, s[6:7] nt
	global_load_dwordx4 v[14:17], v1, s[4:5] nt
	s_cmp_lt_u32 s2, 16
	s_cbranch_scc0 .Lk1_now
	s_load_dwordx2 s[40:41], s[0:1], 0x20
	v_lshl_or_b32 v51, s2, 10, v0
	v_lshrrev_b32_e32 v51, 4, v51
	v_lshrrev_b32_e32 v52, 5, v0
	v_lshlrev_b32_e32 v54, 2, v0
	v_and_b32_e32 v53, 3, v0
	v_and_b32_e32 v51, 0x60, v51
	v_and_or_b32 v53, v54, 16, v53
	v_and_b32_e32 v54, 12, v52
	v_or3_b32 v51, v53, v54, v51
	v_lshlrev_b32_e32 v54, 3, v0
	s_lshl_b32 s44, s2, 4
	v_and_b32_e32 v55, 16, v0
	s_and_b32 s45, s2, -4
	s_and_b32 s44, s44, 32
	v_add_u32_e32 v55, s45, v55
	v_and_or_b32 v54, v54, 64, s44
	v_lshlrev_b32_e32 v51, 7, v51
	v_and_or_b32 v55, v52, 3, v55
	v_add3_u32 v55, v55, v54, v51
	v_lshlrev_b32_e32 v55, 2, v55
	s_waitcnt lgkmcnt(0)
	global_load_dword v51, v55, s[40:41]
.Lk1_now:
	s_movk_i32 s3, 0x7d0
	v_or_b32_e32 v3, 0x400, v0
	v_mov_b32_e32 v2, 0
	v_cmp_gt_u32_e32 vcc, s3, v3
	v_mov_b32_e32 v6, -1
	v_lshlrev_b32_e32 v18, 4, v3
	v_mov_b32_e32 v3, 0
	v_mov_b32_e32 v4, 0
	v_mov_b32_e32 v5, 0
	v_mov_b32_e32 v7, -1
	v_mov_b32_e32 v8, -1
	v_mov_b32_e32 v9, -1
	s_and_saveexec_b64 s[8:9], vcc
	s_cbranch_execz .LBB0_2
	global_load_dwordx4 v[6:9], v18, s[4:5] nt
	global_load_dwordx4 v[2:5], v18, s[6:7] nt

.LBB0_42:
	s_or_b64 exec, exec, s[4:5]
	s_nop 0
	v_lshl_or_b32 v2, s2, 10, v0
	s_movk_i32 s0, 0x4000
	v_cmp_gt_i32_e32 vcc, s0, v2
	v_ashrrev_i32_e32 v3, 31, v2
	s_and_saveexec_b64 s[0:1], vcc
	s_cbranch_execz .LBB0_44
	v_cvt_f16_f32_e32 v4, v51
	v_lshl_add_u64 v[0:1], v[2:3], 1, s[26:27]
	global_store_short v[0:1], v4, off sc1

	.amdhsa_kernel _Z16chunksort_kernelPKiS0_PiS1_PKfPDF16_Pf
		.amdhsa_group_segment_fixed_size 34064
		.amdhsa_private_segment_fixed_size 0
		.amdhsa_kernarg_size 56
		.amdhsa_user_sgpr_count 2
		.amdhsa_user_sgpr_dispatch_ptr 0
		.amdhsa_user_sgpr_queue_ptr 0
		.amdhsa_user_sgpr_kernarg_segment_ptr 1
		.amdhsa_user_sgpr_dispatch_id 0
		.amdhsa_user_sgpr_kernarg_preload_length 0
		.amdhsa_user_sgpr_kernarg_preload_offset 0
		.amdhsa_user_sgpr_private_segment_size 0
		.amdhsa_uses_dynamic_stack 0
		.amdhsa_enable_private_segment 0
		.amdhsa_system_sgpr_workgroup_id_x 1
		.amdhsa_system_sgpr_workgroup_id_y 0
		.amdhsa_system_sgpr_workgroup_id_z 0
		.amdhsa_system_sgpr_workgroup_info 0
		.amdhsa_system_vgpr_workitem_id 0
		.amdhsa_next_free_vgpr 56
		.amdhsa_next_free_sgpr 46
		.amdhsa_accum_offset 56
		.amdhsa_reserve_vcc 1
		.amdhsa_float_round_mode_32 0
		.amdhsa_float_round_mode_16_64 0
		.amdhsa_float_denorm_mode_32 3
		.amdhsa_float_denorm_mode_16_64 3
		.amdhsa_dx10_clamp 1
		.amdhsa_ieee_mode 1
		.amdhsa_fp16_overflow 0
		.amdhsa_tg_split 0
		.amdhsa_exception_fp_ieee_invalid_op 0
		.amdhsa_exception_fp_denorm_src 0
		.amdhsa_exception_fp_ieee_div_zero 0
		.amdhsa_exception_fp_ieee_overflow 0
		.amdhsa_exception_fp_ieee_underflow 0
		.amdhsa_exception_fp_ieee_inexact 0
		.amdhsa_exception_int_div_zero 0
	.end_amdhsa_kernel

.LBB1_4:
	s_or_b64 exec, exec, s[4:5]
	v_mul_u32_u24_e32 v82, 0x1f40, v26
	v_mad_u32_u24 v24, v26, s8, v24
	v_cmp_gt_u32_e64 s[4:5], 4, v0
	s_and_saveexec_b64 s[6:7], s[4:5]
	v_mov_b32_e32 v25, 0x11020
	v_lshl_add_u32 v25, v0, 2, v25
	v_mov_b32_e32 v26, 0
	ds_write_b32 v25, v26
	s_or_b64 exec, exec, s[6:7]
	v_add_u32_e32 v84, v22, v82
	v_max_i32_e32 v22, 1, v83
	v_add_u32_e32 v32, -1, v22
	v_min_u32_e32 v22, v78, v32
	v_add_u32_e32 v22, v22, v84
	v_add_u32_e32 v25, v70, v24
	v_add_u32_e32 v34, v68, v23
	v_ashrrev_i32_e32 v23, 31, v22
	v_or_b32_e32 v24, 16, v78
	s_waitcnt lgkmcnt(0)
	v_lshl_add_u64 v[26:27], v[22:23], 2, s[70:71]
	v_min_u32_e32 v22, v24, v32
	v_add_u32_e32 v22, v22, v84
	v_ashrrev_i32_e32 v23, 31, v22
	v_lshl_add_u64 v[28:29], v[22:23], 2, s[70:71]
	v_or_b32_e32 v23, 32, v78
	v_min_u32_e32 v22, v23, v32
	v_add_u32_e32 v30, v22, v84
	v_ashrrev_i32_e32 v31, 31, v30
	v_or_b32_e32 v22, 48, v78
	v_lshl_add_u64 v[44:45], v[30:31], 2, s[70:71]
	v_min_u32_e32 v30, v22, v32
	v_add_u32_e32 v30, v30, v84
	v_ashrrev_i32_e32 v31, 31, v30
	v_lshl_add_u64 v[46:47], v[30:31], 2, s[70:71]
	v_max_i32_e32 v30, 1, v71
	v_add_u32_e32 v32, -1, v30
	v_min_u32_e32 v30, v78, v32
	v_add_u32_e32 v30, v30, v25
	v_ashrrev_i32_e32 v31, 31, v30
	v_lshl_add_u64 v[48:49], v[30:31], 2, s[70:71]
	v_min_u32_e32 v30, v24, v32
	v_add_u32_e32 v30, v30, v25
	v_ashrrev_i32_e32 v31, 31, v30
	v_lshl_add_u64 v[50:51], v[30:31], 2, s[70:71]
	v_min_u32_e32 v30, v23, v32
	v_add_u32_e32 v30, v30, v25
	v_ashrrev_i32_e32 v31, 31, v30
	v_lshl_add_u64 v[52:53], v[30:31], 2, s[70:71]
	v_min_u32_e32 v30, v22, v32
	v_add_u32_e32 v30, v30, v25
	v_max_i32_e32 v25, 1, v69
	v_ashrrev_i32_e32 v31, 31, v30
	v_add_u32_e32 v25, -1, v25
	v_lshl_add_u64 v[54:55], v[30:31], 2, s[70:71]
	global_load_dword v42, v[26:27], off
	global_load_dword v41, v[28:29], off
	global_load_dword v40, v[44:45], off
	global_load_dword v39, v[46:47], off
	global_load_dword v38, v[48:49], off
	global_load_dword v35, v[50:51], off
	global_load_dword v32, v[52:53], off
	global_load_dword v30, v[54:55], off
	v_min_u32_e32 v26, v78, v25
	v_min_u32_e32 v28, v24, v25
	v_min_u32_e32 v31, v23, v25
	v_min_u32_e32 v25, v22, v25
	v_add_u32_e32 v46, v25, v34
	v_max_i32_e32 v25, 1, v1
	v_add_u32_e32 v25, -1, v25
	v_add_u32_e32 v44, v31, v34
	v_min_u32_e32 v31, v78, v25
	v_add_u32_e32 v48, v31, v21
	v_min_u32_e32 v31, v24, v25
	v_add_u32_e32 v26, v26, v34
	v_add_u32_e32 v28, v28, v34
	v_add_u32_e32 v50, v31, v21
	v_min_u32_e32 v31, v23, v25
	v_min_u32_e32 v25, v22, v25
	v_ashrrev_i32_e32 v27, 31, v26
	v_ashrrev_i32_e32 v29, 31, v28
	v_add_u32_e32 v52, v31, v21
	v_add_u32_e32 v54, v25, v21
	v_lshl_add_u64 v[26:27], v[26:27], 2, s[70:71]
	v_lshl_add_u64 v[28:29], v[28:29], 2, s[70:71]
	v_ashrrev_i32_e32 v45, 31, v44
	v_ashrrev_i32_e32 v47, 31, v46
	v_ashrrev_i32_e32 v49, 31, v48
	v_ashrrev_i32_e32 v51, 31, v50
	v_ashrrev_i32_e32 v53, 31, v52
	v_ashrrev_i32_e32 v55, 31, v54
	v_lshl_add_u64 v[44:45], v[44:45], 2, s[70:71]
	v_lshl_add_u64 v[46:47], v[46:47], 2, s[70:71]
	v_lshl_add_u64 v[48:49], v[48:49], 2, s[70:71]
	v_lshl_add_u64 v[50:51], v[50:51], 2, s[70:71]
	v_lshl_add_u64 v[52:53], v[52:53], 2, s[70:71]
	v_lshl_add_u64 v[54:55], v[54:55], 2, s[70:71]
	global_load_dword v36, v[26:27], off
	global_load_dword v34, v[28:29], off
	global_load_dword v31, v[44:45], off
	s_nop 0
	global_load_dword v29, v[46:47], off
	global_load_dword v28, v[48:49], off
	global_load_dword v27, v[50:51], off
	global_load_dword v26, v[52:53], off
	global_load_dword v25, v[54:55], off
	global_load_dwordx4 v[58:61], v[18:19], off offset:128 nt
	global_load_dwordx4 v[62:65], v[18:19], off offset:192 nt
	global_load_dwordx4 v[50:53], v[18:19], off offset:256 nt
	global_load_dwordx4 v[54:57], v[18:19], off offset:320 nt
	s_load_dwordx2 s[62:63], s[0:1], 0x40
	s_load_dwordx4 s[56:59], s[0:1], 0x20
	s_waitcnt vmcnt(21)
	ds_write_b128 v20, v[10:13]
	s_waitcnt vmcnt(20)
	ds_write_b128 v20, v[14:17] offset:16384
	s_waitcnt lgkmcnt(0)
	s_barrier
	v_bfe_u32 v67, v0, 4, 2
	s_mov_b32 s9, 0
	v_cmp_eq_u32_e64 s[4:5], 0, v78
	s_and_saveexec_b64 s[6:7], s[4:5]
	s_cbranch_execz .LBB1_15
	s_mov_b64 s[4:5], exec

.LBB1_15:
	s_or_b64 exec, exec, s[6:7]
	s_load_dwordx2 s[68:69], s[0:1], 0x48
	s_load_dwordx4 s[64:67], s[0:1], 0x30
	v_cmp_lt_i32_e64 s[0:1], v78, v83
	v_and_b32_e32 v80, 63, v0
	s_waitcnt vmcnt(19)
	v_cndmask_b32_e64 v117, -1, v42, s[0:1]
	v_cmp_lt_i32_e64 s[42:43], -1, v117
	v_lshrrev_b32_e32 v119, 6, v117
	s_and_saveexec_b64 s[0:1], s[42:43]
	s_cbranch_execz .LBB1_17
	v_lshrrev_b32_e32 v10, 15, v117
	v_and_b32_e32 v11, 0x7fc, v119
	v_and_b32_e32 v10, 0x1fffc, v10
	v_or_b32_e32 v11, 0x10800, v11
	v_mov_b32_e32 v12, 1
	v_add_u32_e32 v10, 0x10000, v10
	ds_add_u32 v11, v12
	ds_add_u32 v10, v12
.LBB1_17:
	s_or_b64 exec, exec, s[0:1]
	v_cmp_lt_i32_e64 s[0:1], v24, v83
	s_waitcnt vmcnt(18)
	s_nop 0
	v_cndmask_b32_e64 v115, -1, v41, s[0:1]
	v_cmp_lt_i32_e64 s[50:51], -1, v115
	v_lshrrev_b32_e32 v118, 6, v115
	s_and_saveexec_b64 s[0:1], s[50:51]
	s_cbranch_execz .LBB1_19
	v_lshrrev_b32_e32 v10, 15, v115
	v_and_b32_e32 v11, 0x7fc, v118
	v_and_b32_e32 v10, 0x1fffc, v10
	v_or_b32_e32 v11, 0x10800, v11
	v_mov_b32_e32 v12, 1
	v_add_u32_e32 v10, 0x10000, v10
	ds_add_u32 v11, v12
	ds_add_u32 v10, v12
.LBB1_19:
	s_or_b64 exec, exec, s[0:1]
	v_cmp_lt_i32_e64 s[0:1], v23, v83
	s_waitcnt vmcnt(17)
	s_nop 0
	v_cndmask_b32_e64 v113, -1, v40, s[0:1]
	v_cmp_lt_i32_e64 s[48:49], -1, v113
	v_lshrrev_b32_e32 v116, 6, v113
	s_and_saveexec_b64 s[0:1], s[48:49]
	s_cbranch_execz .LBB1_21
	v_lshrrev_b32_e32 v10, 15, v113
	v_and_b32_e32 v11, 0x7fc, v116
	v_and_b32_e32 v10, 0x1fffc, v10
	v_or_b32_e32 v11, 0x10800, v11
	v_mov_b32_e32 v12, 1
	v_add_u32_e32 v10, 0x10000, v10
	ds_add_u32 v11, v12
	ds_add_u32 v10, v12
.LBB1_21:
	s_or_b64 exec, exec, s[0:1]
	v_cmp_lt_i32_e64 s[0:1], v22, v83
	s_waitcnt vmcnt(16)
	s_nop 0
	v_cndmask_b32_e64 v111, -1, v39, s[0:1]
	v_cmp_lt_i32_e64 s[46:47], -1, v111
	v_lshrrev_b32_e32 v114, 6, v111
	s_and_saveexec_b64 s[0:1], s[46:47]
	s_cbranch_execz .LBB1_23
	v_lshrrev_b32_e32 v10, 15, v111
	v_and_b32_e32 v11, 0x7fc, v114
	v_and_b32_e32 v10, 0x1fffc, v10
	v_or_b32_e32 v11, 0x10800, v11
	v_mov_b32_e32 v12, 1
	v_add_u32_e32 v10, 0x10000, v10
	ds_add_u32 v11, v12
	ds_add_u32 v10, v12
.LBB1_23:
	s_or_b64 exec, exec, s[0:1]
	v_cmp_lt_i32_e64 s[0:1], v78, v71
	s_waitcnt vmcnt(15)
	s_nop 0
	v_cndmask_b32_e64 v109, -1, v38, s[0:1]
	v_cmp_lt_i32_e64 s[44:45], -1, v109
	v_lshrrev_b32_e32 v112, 6, v109
	s_and_saveexec_b64 s[0:1], s[44:45]
	s_cbranch_execz .LBB1_25
	v_lshrrev_b32_e32 v10, 15, v109
	v_and_b32_e32 v11, 0x7fc, v112
	v_and_b32_e32 v10, 0x1fffc, v10
	v_or_b32_e32 v11, 0x10800, v11
	v_mov_b32_e32 v12, 1
	v_add_u32_e32 v10, 0x10000, v10
	ds_add_u32 v11, v12
	ds_add_u32 v10, v12
.LBB1_25:
	s_or_b64 exec, exec, s[0:1]
	v_cmp_lt_i32_e64 s[0:1], v24, v71
	s_waitcnt vmcnt(14)
	s_nop 0
	v_cndmask_b32_e64 v107, -1, v35, s[0:1]
	v_cmp_lt_i32_e64 s[40:41], -1, v107
	v_lshrrev_b32_e32 v110, 6, v107
	s_and_saveexec_b64 s[0:1], s[40:41]
	s_cbranch_execz .LBB1_27
	v_lshrrev_b32_e32 v10, 15, v107
	v_and_b32_e32 v11, 0x7fc, v110
	v_and_b32_e32 v10, 0x1fffc, v10
	v_or_b32_e32 v11, 0x10800, v11
	v_mov_b32_e32 v12, 1
	v_add_u32_e32 v10, 0x10000, v10
	ds_add_u32 v11, v12
	ds_add_u32 v10, v12
.LBB1_27:
	s_or_b64 exec, exec, s[0:1]
	v_cmp_lt_i32_e64 s[0:1], v23, v71
	s_waitcnt vmcnt(13)
	s_nop 0
	v_cndmask_b32_e64 v105, -1, v32, s[0:1]
	v_cmp_lt_i32_e64 s[38:39], -1, v105
	v_lshrrev_b32_e32 v108, 6, v105
	s_and_saveexec_b64 s[0:1], s[38:39]
	s_cbranch_execz .LBB1_29
	v_lshrrev_b32_e32 v10, 15, v105
	v_and_b32_e32 v11, 0x7fc, v108
	v_and_b32_e32 v10, 0x1fffc, v10
	v_or_b32_e32 v11, 0x10800, v11
	v_mov_b32_e32 v12, 1
	v_add_u32_e32 v10, 0x10000, v10
	ds_add_u32 v11, v12
	ds_add_u32 v10, v12
.LBB1_29:
	s_or_b64 exec, exec, s[0:1]
	v_cmp_lt_i32_e64 s[0:1], v22, v71
	s_waitcnt vmcnt(12)
	s_nop 0
	v_cndmask_b32_e64 v103, -1, v30, s[0:1]
	v_cmp_lt_i32_e64 s[36:37], -1, v103
	v_lshrrev_b32_e32 v106, 6, v103
	s_and_saveexec_b64 s[0:1], s[36:37]
	s_cbranch_execz .LBB1_31
	v_lshrrev_b32_e32 v10, 15, v103
	v_and_b32_e32 v11, 0x7fc, v106
	v_and_b32_e32 v10, 0x1fffc, v10
	v_or_b32_e32 v11, 0x10800, v11
	v_mov_b32_e32 v12, 1
	v_add_u32_e32 v10, 0x10000, v10
	ds_add_u32 v11, v12
	ds_add_u32 v10, v12
.LBB1_31:
	s_or_b64 exec, exec, s[0:1]
	v_cmp_lt_i32_e64 s[0:1], v78, v69
	s_waitcnt vmcnt(11)
	s_nop 0
	v_cndmask_b32_e64 v101, -1, v36, s[0:1]
	v_cmp_lt_i32_e64 s[34:35], -1, v101
	v_lshrrev_b32_e32 v104, 6, v101
	s_and_saveexec_b64 s[0:1], s[34:35]
	s_cbranch_execz .LBB1_33
	v_lshrrev_b32_e32 v10, 15, v101
	v_and_b32_e32 v11, 0x7fc, v104
	v_and_b32_e32 v10, 0x1fffc, v10
	v_or_b32_e32 v11, 0x10800, v11
	v_mov_b32_e32 v12, 1
	v_add_u32_e32 v10, 0x10000, v10
	ds_add_u32 v11, v12
	ds_add_u32 v10, v12
.LBB1_33:
	s_or_b64 exec, exec, s[0:1]
	v_cmp_lt_i32_e64 s[0:1], v24, v69
	s_waitcnt vmcnt(10)
	s_nop 0
	v_cndmask_b32_e64 v99, -1, v34, s[0:1]
	v_cmp_lt_i32_e64 s[30:31], -1, v99
	v_lshrrev_b32_e32 v102, 6, v99
	s_and_saveexec_b64 s[0:1], s[30:31]
	s_cbranch_execz .LBB1_35
	v_lshrrev_b32_e32 v10, 15, v99
	v_and_b32_e32 v11, 0x7fc, v102
	v_and_b32_e32 v10, 0x1fffc, v10
	v_or_b32_e32 v11, 0x10800, v11
	v_mov_b32_e32 v12, 1
	v_add_u32_e32 v10, 0x10000, v10
	ds_add_u32 v11, v12
	ds_add_u32 v10, v12
.LBB1_35:
	s_or_b64 exec, exec, s[0:1]
	v_cmp_lt_i32_e64 s[0:1], v23, v69
	s_waitcnt vmcnt(9)
	s_nop 0
	v_cndmask_b32_e64 v97, -1, v31, s[0:1]
	v_cmp_lt_i32_e64 s[28:29], -1, v97
	v_lshrrev_b32_e32 v100, 6, v97
	s_and_saveexec_b64 s[0:1], s[28:29]
	s_cbranch_execz .LBB1_37
	v_lshrrev_b32_e32 v10, 15, v97
	v_and_b32_e32 v11, 0x7fc, v100
	v_and_b32_e32 v10, 0x1fffc, v10
	v_or_b32_e32 v11, 0x10800, v11
	v_mov_b32_e32 v12, 1
	v_add_u32_e32 v10, 0x10000, v10
	ds_add_u32 v11, v12
	ds_add_u32 v10, v12
.LBB1_37:
	s_or_b64 exec, exec, s[0:1]
	v_cmp_lt_i32_e64 s[0:1], v22, v69
	s_waitcnt vmcnt(8)
	s_nop 0
	v_cndmask_b32_e64 v95, -1, v29, s[0:1]
	v_cmp_lt_i32_e64 s[26:27], -1, v95
	v_lshrrev_b32_e32 v98, 6, v95
	s_and_saveexec_b64 s[0:1], s[26:27]
	s_cbranch_execz .LBB1_39
	v_lshrrev_b32_e32 v10, 15, v95
	v_and_b32_e32 v11, 0x7fc, v98
	v_and_b32_e32 v10, 0x1fffc, v10
	v_or_b32_e32 v11, 0x10800, v11
	v_mov_b32_e32 v12, 1
	v_add_u32_e32 v10, 0x10000, v10
	ds_add_u32 v11, v12
	ds_add_u32 v10, v12
.LBB1_39:
	s_or_b64 exec, exec, s[0:1]
	v_cmp_lt_i32_e64 s[0:1], v78, v1
	s_waitcnt vmcnt(7)
	s_nop 0
	v_cndmask_b32_e64 v93, -1, v28, s[0:1]
	v_cmp_lt_i32_e64 s[24:25], -1, v93
	v_lshrrev_b32_e32 v96, 6, v93
	s_and_saveexec_b64 s[0:1], s[24:25]
	s_cbranch_execz .LBB1_41
	v_lshrrev_b32_e32 v10, 15, v93
	v_and_b32_e32 v11, 0x7fc, v96
	v_and_b32_e32 v10, 0x1fffc, v10
	v_or_b32_e32 v11, 0x10800, v11
	v_mov_b32_e32 v12, 1
	v_add_u32_e32 v10, 0x10000, v10
	ds_add_u32 v11, v12
	ds_add_u32 v10, v12
.LBB1_41:
	s_or_b64 exec, exec, s[0:1]
	v_cmp_lt_i32_e64 s[0:1], v24, v1
	s_waitcnt vmcnt(6)
	s_nop 0
	v_cndmask_b32_e64 v91, -1, v27, s[0:1]
	v_cmp_lt_i32_e64 s[22:23], -1, v91
	v_lshrrev_b32_e32 v94, 6, v91
	s_and_saveexec_b64 s[0:1], s[22:23]
	s_cbranch_execz .LBB1_43
	v_lshrrev_b32_e32 v10, 15, v91
	v_and_b32_e32 v11, 0x7fc, v94
	v_and_b32_e32 v10, 0x1fffc, v10
	v_or_b32_e32 v11, 0x10800, v11
	v_mov_b32_e32 v12, 1
	v_add_u32_e32 v10, 0x10000, v10
	ds_add_u32 v11, v12
	ds_add_u32 v10, v12
.LBB1_43:
	s_or_b64 exec, exec, s[0:1]
	v_cmp_lt_i32_e64 s[0:1], v23, v1
	s_waitcnt vmcnt(5)
	s_nop 0
	v_cndmask_b32_e64 v89, -1, v26, s[0:1]
	v_cmp_lt_i32_e64 s[20:21], -1, v89
	v_lshrrev_b32_e32 v92, 6, v89
	s_and_saveexec_b64 s[0:1], s[20:21]
	s_cbranch_execz .LBB1_45
	v_lshrrev_b32_e32 v10, 15, v89
	v_and_b32_e32 v11, 0x7fc, v92
	v_and_b32_e32 v10, 0x1fffc, v10
	v_or_b32_e32 v11, 0x10800, v11
	v_mov_b32_e32 v12, 1
	v_add_u32_e32 v10, 0x10000, v10
	ds_add_u32 v11, v12
	ds_add_u32 v10, v12
.LBB1_45:
	s_or_b64 exec, exec, s[0:1]
	v_cmp_lt_i32_e64 s[0:1], v22, v1
	s_waitcnt vmcnt(4)
	s_nop 0
	v_cndmask_b32_e64 v87, -1, v25, s[0:1]
	v_cmp_lt_i32_e64 s[18:19], -1, v87
	v_lshrrev_b32_e32 v90, 6, v87
	s_and_saveexec_b64 s[0:1], s[18:19]
	s_cbranch_execz .LBB1_47
	v_lshrrev_b32_e32 v10, 15, v87
	v_and_b32_e32 v11, 0x7fc, v90
	v_and_b32_e32 v10, 0x1fffc, v10
	v_or_b32_e32 v11, 0x10800, v11
	v_mov_b32_e32 v12, 1
	v_add_u32_e32 v10, 0x10000, v10
	ds_add_u32 v11, v12
	ds_add_u32 v10, v12

.LBB1_61:
	s_or_b64 exec, exec, s[6:7]
	v_or_b32_e32 v12, 0x100, v66
	v_add_u32_e32 v10, s54, v12
	v_ashrrev_i32_e32 v11, 31, v10
	v_lshlrev_b64 v[10:11], 7, v[10:11]
	v_cmp_gt_i32_e64 s[4:5], s3, v12
	v_mov_b32_e32 v77, 0
	v_lshlrev_b32_e32 v76, 4, v67
	v_cndmask_b32_e64 v11, 0, v11, s[4:5]
	v_cndmask_b32_e64 v10, 0, v10, s[4:5]
	v_lshl_add_u64 v[10:11], v[10:11], 2, s[60:61]
	v_lshl_add_u64 v[14:15], v[10:11], 0, v[76:77]
	global_load_dwordx4 v[42:45], v[18:19], off offset:384 nt
	global_load_dwordx4 v[46:49], v[18:19], off offset:448 nt
	global_load_dwordx4 v[34:37], v[14:15], off nt
	global_load_dwordx4 v[38:41], v[14:15], off offset:64 nt
	global_load_dwordx4 v[26:29], v[14:15], off offset:128 nt
	global_load_dwordx4 v[30:33], v[14:15], off offset:192 nt
	s_nop 0
	global_load_dwordx4 v[18:21], v[14:15], off offset:256 nt
	global_load_dwordx4 v[22:25], v[14:15], off offset:320 nt
	global_load_dwordx4 v[10:13], v[14:15], off offset:384 nt
	s_nop 0
	global_load_dwordx4 v[14:17], v[14:15], off offset:448 nt
	s_waitcnt lgkmcnt(0)
	s_barrier
	v_mov_b32_e32 v73, 0x11020
	ds_read_b64 v[120:121], v73
	v_mbcnt_lo_u32_b32 v81, -1, 0
	v_mov_b32_e32 v73, v77
	s_waitcnt lgkmcnt(0)
	v_readfirstlane_b32 s33, v120
	v_readfirstlane_b32 s55, v121
	s_and_saveexec_b64 s[60:61], vcc
	s_cbranch_execz .LBB1_65
	v_mov_b32_e32 v73, 0x10800
	v_lshl_add_u32 v73, v0, 2, v73
	ds_read_b32 v77, v73
	v_mbcnt_hi_u32_b32 v73, -1, v81
	v_and_b32_e32 v75, 64, v73
	v_add_u32_e32 v76, -1, v73
	v_cmp_lt_i32_e64 s[6:7], v76, v75
	v_add_u32_e32 v120, -2, v73
	s_nop 0
	v_cndmask_b32_e64 v76, v76, v73, s[6:7]
	v_lshlrev_b32_e32 v76, 2, v76
	s_waitcnt lgkmcnt(0)
	ds_bpermute_b32 v76, v76, v77
	v_cmp_ne_u32_e64 s[6:7], 0, v80
	s_waitcnt lgkmcnt(0)
	s_nop 0
	v_cndmask_b32_e64 v76, 0, v76, s[6:7]
	v_cmp_lt_i32_e64 s[6:7], v120, v75
	v_add_u32_e32 v76, v76, v77
	s_nop 0
	v_cndmask_b32_e64 v120, v120, v73, s[6:7]
	v_lshlrev_b32_e32 v120, 2, v120
	ds_bpermute_b32 v120, v120, v76
	v_cmp_lt_u32_e64 s[6:7], 1, v80
	s_waitcnt lgkmcnt(0)
	s_nop 0
	v_cndmask_b32_e64 v120, 0, v120, s[6:7]
	v_add_u32_e32 v76, v120, v76
	v_add_u32_e32 v120, -4, v73
	v_cmp_lt_i32_e64 s[6:7], v120, v75
	s_nop 1
	v_cndmask_b32_e64 v120, v120, v73, s[6:7]
	v_lshlrev_b32_e32 v120, 2, v120
	ds_bpermute_b32 v120, v120, v76
	v_cmp_lt_u32_e64 s[6:7], 3, v80
	s_waitcnt lgkmcnt(0)
	s_nop 0
	v_cndmask_b32_e64 v120, 0, v120, s[6:7]
	v_add_u32_e32 v76, v120, v76
	v_add_u32_e32 v120, -8, v73
	v_cmp_lt_i32_e64 s[6:7], v120, v75
	s_nop 1
	v_cndmask_b32_e64 v120, v120, v73, s[6:7]
	v_lshlrev_b32_e32 v120, 2, v120
	ds_bpermute_b32 v120, v120, v76
	v_cmp_lt_u32_e64 s[6:7], 7, v80
	s_waitcnt lgkmcnt(0)
	s_nop 0
	v_cndmask_b32_e64 v120, 0, v120, s[6:7]
	v_add_u32_e32 v76, v120, v76
	v_add_u32_e32 v120, -16, v73
	v_cmp_lt_i32_e64 s[6:7], v120, v75
	s_nop 1
	v_cndmask_b32_e64 v120, v120, v73, s[6:7]
	v_lshlrev_b32_e32 v120, 2, v120
	ds_bpermute_b32 v120, v120, v76
	v_cmp_lt_u32_e64 s[6:7], 15, v80
	s_waitcnt lgkmcnt(0)
	s_nop 0
	v_cndmask_b32_e64 v120, 0, v120, s[6:7]
	v_add_u32_e32 v76, v120, v76
	v_subrev_u32_e32 v120, 32, v73
	v_cmp_lt_i32_e64 s[6:7], v120, v75
	s_nop 1
	v_cndmask_b32_e64 v73, v120, v73, s[6:7]
	v_lshlrev_b32_e32 v73, 2, v73
	ds_bpermute_b32 v73, v73, v76
	v_cmp_lt_u32_e64 s[6:7], 31, v80
	s_waitcnt lgkmcnt(0)
	s_nop 0
	v_cndmask_b32_e64 v73, 0, v73, s[6:7]
	v_add_u32_e32 v73, v73, v76
	v_cmp_eq_u32_e64 s[6:7], 63, v80
	s_and_saveexec_b64 s[72:73], s[6:7]
	v_mov_b32_e32 v75, 0x11000
	v_lshl_or_b32 v75, v79, 2, v75
	ds_write_b32 v75, v73
	s_or_b64 exec, exec, s[72:73]

_Z10agg_kernelPKDF16_PKiS2_S2_PKfS2_PDF16_Pfi:
	s_load_dwordx8 s[12:19], s[0:1], 0x0
	s_lshl_b32 s4, s2, 1
	s_ashr_i32 s5, s4, 31
	s_lshl_b64 s[4:5], s[4:5], 2
	v_and_b32_e32 v1, 63, v0
	s_waitcnt lgkmcnt(0)
	s_add_u32 s20, s16, s4
	s_addc_u32 s21, s17, s5
	s_load_dwordx2 s[16:17], s[20:21], 0x0
	s_load_dwordx8 s[4:11], s[0:1], 0x20
	v_readfirstlane_b32 s3, v0
	v_lshlrev_b32_e32 v2, 2, v1
	s_lshr_b32 s3, s3, 6
	s_waitcnt lgkmcnt(0)
	s_ashr_i32 s21, s16, 31
	s_mov_b32 s20, s16
	global_load_dword v3, v2, s[6:7]
	global_load_dword v4, v2, s[6:7] offset:256
	global_load_dword v6, v2, s[6:7] offset:512
	global_load_dword v5, v2, s[6:7] offset:768
	s_lshl_b64 s[6:7], s[20:21], 2
	s_add_u32 s6, s14, s6
	s_addc_u32 s7, s15, s7
	s_add_i32 s21, s17, 15
	s_ashr_i32 s21, s21, 4
	s_max_i32 s20, s21, 1
	s_add_i32 s20, s20, -1
	s_min_u32 s14, s3, s20
	s_bfe_u32 s44, s2, 0x10002
	s_mul_i32 s45, s44, s20
	s_lshl_b32 s44, s44, 1
	s_sub_i32 s44, 1, s44
	s_mul_i32 s14, s14, s44
	s_add_i32 s14, s14, s45
	s_lshl_b32 s30, s14, 4
	v_mov_b32_e32 v59, 0x30e0000
	v_bfe_u32 v2, v0, 4, 2
	v_lshlrev_b32_e32 v7, 2, v0
	s_lshl_b32 s14, s14, 6
	v_and_or_b32 v18, v7, 12, v2
	s_add_u32 s14, s6, s14
	s_addc_u32 s15, s7, 0
	v_lshlrev_b32_e32 v2, 2, v18
	global_load_dword v2, v2, s[14:15]
	v_lshlrev_b32_e32 v20, 2, v18
	v_mov_b32_e32 v8, 0
	v_mov_b32_e32 v9, 0
	v_mov_b32_e32 v10, 0
	v_mov_b32_e32 v11, 0
	v_lshlrev_b32_e32 v12, 4, v0
	v_add_u32_e32 v13, 0x10000, v12
	ds_write_b128 v12, v[8:11]
	ds_write_b128 v12, v[8:11] offset:16384
	ds_write_b128 v12, v[8:11] offset:32768
	ds_write_b128 v12, v[8:11] offset:49152
	ds_write_b128 v13, v[8:11]
	ds_write_b128 v13, v[8:11] offset:16384
	ds_write_b128 v13, v[8:11] offset:32768
	v_cmp_gt_u32_e32 vcc, 0x28c, v0
	s_and_saveexec_b64 s[14:15], vcc
	ds_write_b128 v13, v[8:11] offset:49152
	s_or_b64 exec, exec, s[14:15]
	s_waitcnt vmcnt(2)
	v_max3_i32 v3, v3, v4, v6
	v_mbcnt_lo_u32_b32 v4, -1, 0
	v_mbcnt_hi_u32_b32 v4, -1, v4
	v_and_b32_e32 v25, 64, v4
	s_waitcnt vmcnt(1)
	v_max3_i32 v3, v3, v5, 0
	v_add_u32_e32 v5, 64, v25
	v_xor_b32_e32 v6, 1, v4
	v_cmp_lt_i32_e32 vcc, v6, v5
	s_load_dword s16, s[0:1], 0x40
	s_mul_i32 s14, s2, 0x187
	v_cndmask_b32_e32 v6, v4, v6, vcc
	v_lshlrev_b32_e32 v6, 2, v6
	ds_bpermute_b32 v6, v6, v3
	s_waitcnt lgkmcnt(0)
	s_sub_i32 s15, s16, s14
	s_movk_i32 s0, 0x73
	s_cmp_gt_i32 s21, s3
	s_cselect_b64 s[22:23], -1, 0
	v_max_i32_e32 v3, v3, v6
	v_xor_b32_e32 v6, 2, v4
	v_cmp_lt_i32_e32 vcc, v6, v5
	v_mov_b32_e32 v29, 0
	v_mov_b32_e32 v27, 0
	v_cndmask_b32_e32 v6, v4, v6, vcc
	v_lshlrev_b32_e32 v6, 2, v6
	ds_bpermute_b32 v6, v6, v3
	v_mov_b32_e32 v28, 0
	v_mov_b32_e32 v26, 0
	v_mov_b32_e32 v21, 0
	s_waitcnt lgkmcnt(0)
	v_max_i32_e32 v3, v3, v6
	v_xor_b32_e32 v6, 4, v4
	v_cmp_lt_i32_e32 vcc, v6, v5
	v_cndmask_b32_e32 v6, v4, v6, vcc
	v_lshlrev_b32_e32 v6, 2, v6
	ds_bpermute_b32 v6, v6, v3
	s_waitcnt lgkmcnt(0)
	s_barrier
	v_max_i32_e32 v3, v3, v6
	v_xor_b32_e32 v6, 8, v4
	v_cmp_lt_i32_e32 vcc, v6, v5
	s_nop 1
	v_cndmask_b32_e32 v6, v4, v6, vcc
	v_lshlrev_b32_e32 v60, 2, v6
	ds_bpermute_b32 v6, v60, v3
	s_waitcnt lgkmcnt(0)
	v_max_i32_e32 v3, v3, v6
	v_xor_b32_e32 v6, 16, v4
	v_cmp_lt_i32_e32 vcc, v6, v5
	s_nop 1
	v_cndmask_b32_e32 v6, v4, v6, vcc
	v_lshlrev_b32_e32 v61, 2, v6
	ds_bpermute_b32 v6, v61, v3
	s_waitcnt lgkmcnt(0)
	v_max_i32_e32 v3, v3, v6
	v_xor_b32_e32 v6, 32, v4
	v_cmp_lt_i32_e32 vcc, v6, v5
	v_and_b32_e32 v5, 15, v0
	v_lshlrev_b32_e32 v24, 4, v5
	v_cndmask_b32_e32 v4, v4, v6, vcc
	v_lshlrev_b32_e32 v66, 2, v4
	ds_bpermute_b32 v4, v66, v3
	v_lshlrev_b32_e32 v23, 2, v5
	s_waitcnt lgkmcnt(0)
	v_max_i32_e32 v3, v3, v4
	v_lshrrev_b32_e32 v3, 23, v3
	v_mov_b32_e32 v4, 0x8b
	v_med3_u32 v3, v3, s0, v4
	s_sub_i32 s0, s21, s3
	s_add_i32 s0, s0, 15
	s_cmp_gt_u32 s0, 15
	s_cselect_b64 s[24:25], -1, 0
	v_lshlrev_b32_e32 v19, 23, v3
	s_and_b64 s[22:23], s[22:23], s[24:25]
	v_sub_u32_e32 v22, 0x84800000, v19
	s_waitcnt vmcnt(0)
	v_add_u32_e32 v33, s30, v18
	v_cmp_gt_i32_e64 s[28:29], s17, v33
	s_nop 1
	v_cndmask_b32_e64 v2, v59, v2, s[28:29]
	s_nop 1
	v_mov_b32_dpp v29, v2 row_newbcast:0 row_mask:0xf bank_mask:0xf
	v_mov_b32_dpp v27, v2 row_newbcast:1 row_mask:0xf bank_mask:0xf
	v_mov_b32_dpp v28, v2 row_newbcast:2 row_mask:0xf bank_mask:0xf
	v_mov_b32_dpp v26, v2 row_newbcast:3 row_mask:0xf bank_mask:0xf
	s_and_b64 vcc, exec, s[22:23]
	s_cbranch_vccz .LBB2_5
	s_lshr_b32 s21, s0, 4
	s_mov_b32 s1, 0
	s_mov_b32 s22, 0x1ffff00
	s_mov_b32 s23, 0x4b400000
	v_lshl_add_u64 v[20:21], s[6:7], 0, v[20:21]
	s_add_i32 s0, s3, 16
	s_mov_b32 s24, s0
	s_min_i32 s24, s24, s20
	s_mul_i32 s24, s24, s44
	s_add_i32 s24, s24, s45
	s_lshl_b32 s24, s24, 4
	s_ashr_i32 s25, s24, 31
	v_lshl_add_u64 v[32:33], s[24:25], 2, v[20:21]
	global_load_dword v30, v[32:33], off
	v_lshlrev_b32_e32 v35, 8, v29
	v_and_or_b32 v35, v35, s22, v24
	global_load_dwordx4 v[2:5], v35, s[12:13]
	v_lshlrev_b32_e32 v35, 8, v27
	v_and_or_b32 v35, v35, s22, v24
	global_load_dwordx4 v[6:9], v35, s[12:13]
	v_lshlrev_b32_e32 v35, 8, v28
	v_and_or_b32 v35, v35, s22, v24
	global_load_dwordx4 v[10:13], v35, s[12:13]
	v_lshlrev_b32_e32 v35, 8, v26
	v_and_or_b32 v35, v35, s22, v24
	global_load_dwordx4 v[14:17], v35, s[12:13]
